# indexer ordered-emission pass: 60 of 64 per-key blocks made branch-free (two compares, one predicated store, carry-in counter updates) instead of 4 nested exec branches per key; on top of packed keys
# speedup vs baseline: 1.0134x; 1.0134x over previous
.LBB0_718:
	v_lshl_add_u64 v[8:9], v[6:7], 1, s[12:13]
	global_load_dwordx4 v[4:7], v[8:9], off offset:16
	s_nop 0
	global_load_dwordx4 v[8:11], v[8:9], off
	s_and_saveexec_b64 s[24:25], vcc
	s_cbranch_execz .LBB0_845
	ds_read_u16 v2, v49 offset:36864
	v_add_u32_e32 v44, 0x11200, v49
	ds_read_b32 v44, v44
	s_waitcnt vmcnt(6)
	s_waitcnt lgkmcnt(1)
	v_lshrrev_b32_e32 v45, 8, v2
	v_and_b32_e32 v2, 0xff, v2
	v_cndmask_b32_e64 v45, v45, 0, s[22:23]
	v_cndmask_b32_e64 v2, v2, 0, s[22:23]
	s_waitcnt lgkmcnt(0)
	v_add_u32_sdwa v51, v45, v44 dst_sel:DWORD dst_unused:UNUSED_PAD src0_sel:DWORD src1_sel:WORD_1
	v_add_u32_sdwa v214, v2, v44 dst_sel:DWORD dst_unused:UNUSED_PAD src0_sel:DWORD src1_sel:WORD_0
	v_lshl_add_u64 v[44:45], v[40:41], 0, s[16:17]
	v_cmp_gt_u32_sdwa s[0:1], v32, v36 src0_sel:WORD_0 src1_sel:DWORD
	v_cmp_eq_u32_sdwa s[30:31], v32, v36 src0_sel:WORD_0 src1_sel:DWORD
	v_cmp_lt_i32_e32 vcc, v51, v37
	v_min_i32_e32 v2, v51, v37
	v_add_u32_e32 v2, v2, v214
	s_and_b64 vcc, vcc, s[30:31]
	s_or_b64 vcc, vcc, s[0:1]
	v_lshl_add_u64 v[46:47], v[2:3], 1, v[38:39]
	s_and_saveexec_b64 s[34:35], vcc
	global_store_short v[46:47], v44, off
	s_mov_b64 exec, s[34:35]
	v_addc_co_u32_e64 v214, vcc, 0, v214, s[0:1]
	v_addc_co_u32_e64 v51, vcc, 0, v51, s[30:31]
	v_lshl_add_u64 v[46:47], v[44:45], 0, 1
	v_cmp_gt_u32_sdwa s[0:1], v32, v36 src0_sel:WORD_1 src1_sel:DWORD
	v_cmp_eq_u32_sdwa s[30:31], v32, v36 src0_sel:WORD_1 src1_sel:DWORD
	v_cmp_lt_i32_e32 vcc, v51, v37
	v_min_i32_e32 v2, v51, v37
	v_add_u32_e32 v2, v2, v214
	s_and_b64 vcc, vcc, s[30:31]
	s_or_b64 vcc, vcc, s[0:1]
	v_lshl_add_u64 v[212:213], v[2:3], 1, v[38:39]
	s_and_saveexec_b64 s[34:35], vcc
	global_store_short v[212:213], v46, off
	s_mov_b64 exec, s[34:35]
	v_addc_co_u32_e64 v214, vcc, 0, v214, s[0:1]
	v_addc_co_u32_e64 v51, vcc, 0, v51, s[30:31]
	v_lshl_add_u64 v[46:47], v[44:45], 0, 2
	v_cmp_gt_u32_sdwa s[0:1], v33, v36 src0_sel:WORD_0 src1_sel:DWORD
	v_cmp_eq_u32_sdwa s[30:31], v33, v36 src0_sel:WORD_0 src1_sel:DWORD
	v_cmp_lt_i32_e32 vcc, v51, v37
	v_min_i32_e32 v2, v51, v37
	v_add_u32_e32 v2, v2, v214
	s_and_b64 vcc, vcc, s[30:31]
	s_or_b64 vcc, vcc, s[0:1]
	v_lshl_add_u64 v[212:213], v[2:3], 1, v[38:39]
	s_and_saveexec_b64 s[34:35], vcc
	global_store_short v[212:213], v46, off
	s_mov_b64 exec, s[34:35]
	v_addc_co_u32_e64 v214, vcc, 0, v214, s[0:1]
	v_addc_co_u32_e64 v51, vcc, 0, v51, s[30:31]
	v_lshl_add_u64 v[46:47], v[44:45], 0, 3
	v_cmp_gt_u32_sdwa s[0:1], v33, v36 src0_sel:WORD_1 src1_sel:DWORD
	v_cmp_eq_u32_sdwa s[30:31], v33, v36 src0_sel:WORD_1 src1_sel:DWORD
	v_cmp_lt_i32_e32 vcc, v51, v37
	v_min_i32_e32 v2, v51, v37
	v_add_u32_e32 v2, v2, v214
	s_and_b64 vcc, vcc, s[30:31]
	s_or_b64 vcc, vcc, s[0:1]
	v_lshl_add_u64 v[32:33], v[2:3], 1, v[38:39]
	s_and_saveexec_b64 s[34:35], vcc
	global_store_short v[32:33], v46, off
	s_mov_b64 exec, s[34:35]
	v_addc_co_u32_e64 v214, vcc, 0, v214, s[0:1]
	v_addc_co_u32_e64 v51, vcc, 0, v51, s[30:31]
	v_lshl_add_u64 v[32:33], v[44:45], 0, 4
	v_cmp_gt_u32_sdwa s[0:1], v34, v36 src0_sel:WORD_0 src1_sel:DWORD
	v_cmp_eq_u32_sdwa s[30:31], v34, v36 src0_sel:WORD_0 src1_sel:DWORD
	v_cmp_lt_i32_e32 vcc, v51, v37
	v_min_i32_e32 v2, v51, v37
	v_add_u32_e32 v2, v2, v214
	s_and_b64 vcc, vcc, s[30:31]
	s_or_b64 vcc, vcc, s[0:1]
	v_lshl_add_u64 v[46:47], v[2:3], 1, v[38:39]
	s_and_saveexec_b64 s[34:35], vcc
	global_store_short v[46:47], v32, off
	s_mov_b64 exec, s[34:35]
	v_addc_co_u32_e64 v214, vcc, 0, v214, s[0:1]
	v_addc_co_u32_e64 v51, vcc, 0, v51, s[30:31]
	v_lshl_add_u64 v[32:33], v[44:45], 0, 5
	v_cmp_gt_u32_sdwa s[0:1], v34, v36 src0_sel:WORD_1 src1_sel:DWORD
	v_cmp_eq_u32_sdwa s[30:31], v34, v36 src0_sel:WORD_1 src1_sel:DWORD
	v_cmp_lt_i32_e32 vcc, v51, v37
	v_min_i32_e32 v2, v51, v37
	v_add_u32_e32 v2, v2, v214
	s_and_b64 vcc, vcc, s[30:31]
	s_or_b64 vcc, vcc, s[0:1]
	v_lshl_add_u64 v[46:47], v[2:3], 1, v[38:39]
	s_and_saveexec_b64 s[34:35], vcc
	global_store_short v[46:47], v32, off
	s_mov_b64 exec, s[34:35]
	v_addc_co_u32_e64 v214, vcc, 0, v214, s[0:1]
	v_addc_co_u32_e64 v51, vcc, 0, v51, s[30:31]
	v_lshl_add_u64 v[32:33], v[44:45], 0, 6
	v_cmp_gt_u32_sdwa s[0:1], v35, v36 src0_sel:WORD_0 src1_sel:DWORD
	v_cmp_eq_u32_sdwa s[30:31], v35, v36 src0_sel:WORD_0 src1_sel:DWORD
	v_cmp_lt_i32_e32 vcc, v51, v37
	v_min_i32_e32 v2, v51, v37
	v_add_u32_e32 v2, v2, v214
	s_and_b64 vcc, vcc, s[30:31]
	s_or_b64 vcc, vcc, s[0:1]
	v_lshl_add_u64 v[46:47], v[2:3], 1, v[38:39]
	s_and_saveexec_b64 s[34:35], vcc
	global_store_short v[46:47], v32, off
	s_mov_b64 exec, s[34:35]
	v_addc_co_u32_e64 v214, vcc, 0, v214, s[0:1]
	v_addc_co_u32_e64 v51, vcc, 0, v51, s[30:31]
	v_lshl_add_u64 v[32:33], v[44:45], 0, 7
	v_cmp_gt_u32_sdwa s[0:1], v35, v36 src0_sel:WORD_1 src1_sel:DWORD
	v_cmp_eq_u32_sdwa s[30:31], v35, v36 src0_sel:WORD_1 src1_sel:DWORD
	v_cmp_lt_i32_e32 vcc, v51, v37
	v_min_i32_e32 v2, v51, v37
	v_add_u32_e32 v2, v2, v214
	s_and_b64 vcc, vcc, s[30:31]
	s_or_b64 vcc, vcc, s[0:1]
	v_lshl_add_u64 v[34:35], v[2:3], 1, v[38:39]
	s_and_saveexec_b64 s[34:35], vcc
	global_store_short v[34:35], v32, off
	s_mov_b64 exec, s[34:35]
	v_addc_co_u32_e64 v214, vcc, 0, v214, s[0:1]
	v_addc_co_u32_e64 v51, vcc, 0, v51, s[30:31]
	v_lshl_add_u64 v[32:33], v[44:45], 0, 8
	v_cmp_gt_u32_sdwa s[0:1], v28, v36 src0_sel:WORD_0 src1_sel:DWORD
	v_cmp_eq_u32_sdwa s[30:31], v28, v36 src0_sel:WORD_0 src1_sel:DWORD
	v_cmp_lt_i32_e32 vcc, v51, v37
	v_min_i32_e32 v2, v51, v37
	v_add_u32_e32 v2, v2, v214
	s_and_b64 vcc, vcc, s[30:31]
	s_or_b64 vcc, vcc, s[0:1]
	v_lshl_add_u64 v[34:35], v[2:3], 1, v[38:39]
	s_and_saveexec_b64 s[34:35], vcc
	global_store_short v[34:35], v32, off
	s_mov_b64 exec, s[34:35]
	v_addc_co_u32_e64 v214, vcc, 0, v214, s[0:1]
	v_addc_co_u32_e64 v51, vcc, 0, v51, s[30:31]
	v_lshl_add_u64 v[32:33], v[44:45], 0, 9
	v_cmp_gt_u32_sdwa s[0:1], v28, v36 src0_sel:WORD_1 src1_sel:DWORD
	v_cmp_eq_u32_sdwa s[30:31], v28, v36 src0_sel:WORD_1 src1_sel:DWORD
	v_cmp_lt_i32_e32 vcc, v51, v37
	v_min_i32_e32 v2, v51, v37
	v_add_u32_e32 v2, v2, v214
	s_and_b64 vcc, vcc, s[30:31]
	s_or_b64 vcc, vcc, s[0:1]
	v_lshl_add_u64 v[34:35], v[2:3], 1, v[38:39]
	s_and_saveexec_b64 s[34:35], vcc
	global_store_short v[34:35], v32, off
	s_mov_b64 exec, s[34:35]
	v_addc_co_u32_e64 v214, vcc, 0, v214, s[0:1]
	v_addc_co_u32_e64 v51, vcc, 0, v51, s[30:31]
	v_lshl_add_u64 v[32:33], v[44:45], 0, 10
	v_cmp_gt_u32_sdwa s[0:1], v29, v36 src0_sel:WORD_0 src1_sel:DWORD
	v_cmp_eq_u32_sdwa s[30:31], v29, v36 src0_sel:WORD_0 src1_sel:DWORD
	v_cmp_lt_i32_e32 vcc, v51, v37
	v_min_i32_e32 v2, v51, v37
	v_add_u32_e32 v2, v2, v214
	s_and_b64 vcc, vcc, s[30:31]
	s_or_b64 vcc, vcc, s[0:1]
	v_lshl_add_u64 v[34:35], v[2:3], 1, v[38:39]
	s_and_saveexec_b64 s[34:35], vcc
	global_store_short v[34:35], v32, off
	s_mov_b64 exec, s[34:35]
	v_addc_co_u32_e64 v214, vcc, 0, v214, s[0:1]
	v_addc_co_u32_e64 v51, vcc, 0, v51, s[30:31]
	v_lshl_add_u64 v[32:33], v[44:45], 0, 11
	v_cmp_gt_u32_sdwa s[0:1], v29, v36 src0_sel:WORD_1 src1_sel:DWORD
	v_cmp_eq_u32_sdwa s[30:31], v29, v36 src0_sel:WORD_1 src1_sel:DWORD
	v_cmp_lt_i32_e32 vcc, v51, v37
	v_min_i32_e32 v2, v51, v37
	v_add_u32_e32 v2, v2, v214
	s_and_b64 vcc, vcc, s[30:31]
	s_or_b64 vcc, vcc, s[0:1]
	v_lshl_add_u64 v[28:29], v[2:3], 1, v[38:39]
	s_and_saveexec_b64 s[34:35], vcc
	global_store_short v[28:29], v32, off
	s_mov_b64 exec, s[34:35]
	v_addc_co_u32_e64 v214, vcc, 0, v214, s[0:1]
	v_addc_co_u32_e64 v51, vcc, 0, v51, s[30:31]
	v_lshl_add_u64 v[28:29], v[44:45], 0, 12
	v_cmp_gt_u32_sdwa s[0:1], v30, v36 src0_sel:WORD_0 src1_sel:DWORD
	v_cmp_eq_u32_sdwa s[30:31], v30, v36 src0_sel:WORD_0 src1_sel:DWORD
	v_cmp_lt_i32_e32 vcc, v51, v37
	v_min_i32_e32 v2, v51, v37
	v_add_u32_e32 v2, v2, v214
	s_and_b64 vcc, vcc, s[30:31]
	s_or_b64 vcc, vcc, s[0:1]
	v_lshl_add_u64 v[32:33], v[2:3], 1, v[38:39]
	s_and_saveexec_b64 s[34:35], vcc
	global_store_short v[32:33], v28, off
	s_mov_b64 exec, s[34:35]
	v_addc_co_u32_e64 v214, vcc, 0, v214, s[0:1]
	v_addc_co_u32_e64 v51, vcc, 0, v51, s[30:31]
	v_lshl_add_u64 v[28:29], v[44:45], 0, 13
	v_cmp_gt_u32_sdwa s[0:1], v30, v36 src0_sel:WORD_1 src1_sel:DWORD
	v_cmp_eq_u32_sdwa s[30:31], v30, v36 src0_sel:WORD_1 src1_sel:DWORD
	v_cmp_lt_i32_e32 vcc, v51, v37
	v_min_i32_e32 v2, v51, v37
	v_add_u32_e32 v2, v2, v214
	s_and_b64 vcc, vcc, s[30:31]
	s_or_b64 vcc, vcc, s[0:1]
	v_lshl_add_u64 v[32:33], v[2:3], 1, v[38:39]
	s_and_saveexec_b64 s[34:35], vcc
	global_store_short v[32:33], v28, off
	s_mov_b64 exec, s[34:35]
	v_addc_co_u32_e64 v214, vcc, 0, v214, s[0:1]
	v_addc_co_u32_e64 v51, vcc, 0, v51, s[30:31]
	v_lshl_add_u64 v[28:29], v[44:45], 0, 14
	v_cmp_gt_u32_sdwa s[0:1], v31, v36 src0_sel:WORD_0 src1_sel:DWORD
	v_cmp_eq_u32_sdwa s[30:31], v31, v36 src0_sel:WORD_0 src1_sel:DWORD
	v_cmp_lt_i32_e32 vcc, v51, v37
	v_min_i32_e32 v2, v51, v37
	v_add_u32_e32 v2, v2, v214
	s_and_b64 vcc, vcc, s[30:31]
	s_or_b64 vcc, vcc, s[0:1]
	v_lshl_add_u64 v[32:33], v[2:3], 1, v[38:39]
	s_and_saveexec_b64 s[34:35], vcc
	global_store_short v[32:33], v28, off
	s_mov_b64 exec, s[34:35]
	v_addc_co_u32_e64 v214, vcc, 0, v214, s[0:1]
	v_addc_co_u32_e64 v51, vcc, 0, v51, s[30:31]
	v_cmp_le_u32_sdwa s[30:31], v31, v36 src0_sel:WORD_1 src1_sel:DWORD
	s_mov_b64 s[0:1], 0
	s_and_saveexec_b64 s[34:35], s[30:31]
	s_xor_b64 s[30:31], exec, s[34:35]
	s_cbranch_execz .LBB0_1230
	v_cmp_eq_u32_sdwa s[0:1], v31, v36 src0_sel:WORD_1 src1_sel:DWORD
	v_cmp_lt_i32_e32 vcc, v51, v37
	s_and_b64 s[38:39], s[0:1], vcc
	s_mov_b64 s[0:1], 0
	s_and_saveexec_b64 s[34:35], s[38:39]
	v_add_u32_e32 v2, v51, v214
	s_mov_b64 s[0:1], exec
	v_mov_b64_e32 v[28:29], v[2:3]
	s_or_b64 exec, exec, s[34:35]
	s_and_b64 s[0:1], s[0:1], exec
	s_andn2_saveexec_b64 s[30:31], s[30:31]
	s_cbranch_execnz .LBB0_1231

.LBB0_845:
	s_or_b64 exec, exec, s[24:25]
	s_andn2_b64 vcc, exec, s[18:19]
	s_cbranch_vccnz .LBB0_975
	ds_read_u16 v2, v50 offset:36896
	s_waitcnt lgkmcnt(0)
	v_cmp_ne_u16_e32 vcc, 0, v2
	s_and_saveexec_b64 s[18:19], vcc
	s_cbranch_execz .LBB0_973
	ds_read_u16 v2, v49 offset:36896
	s_waitcnt vmcnt(7)
	v_add_u32_e32 v28, 0x11220, v49
	ds_read_b32 v28, v28
	v_lshl_add_u64 v[30:31], v[40:41], 0, s[16:17]
	s_waitcnt vmcnt(4)
	s_waitcnt lgkmcnt(1)
	v_lshrrev_b32_e32 v29, 8, v2
	v_and_b32_e32 v2, 0xff, v2
	v_cndmask_b32_e64 v29, v29, 0, s[22:23]
	v_cndmask_b32_e64 v2, v2, 0, s[22:23]
	s_waitcnt lgkmcnt(0)
	v_add_u32_sdwa v34, v29, v28 dst_sel:DWORD dst_unused:UNUSED_PAD src0_sel:DWORD src1_sel:WORD_1
	v_add_u32_sdwa v35, v2, v28 dst_sel:DWORD dst_unused:UNUSED_PAD src0_sel:DWORD src1_sel:WORD_0
	v_lshl_add_u64 v[28:29], v[30:31], 0, s[84:85]
	v_cmp_gt_u32_sdwa s[0:1], v24, v36 src0_sel:WORD_0 src1_sel:DWORD
	v_cmp_eq_u32_sdwa s[24:25], v24, v36 src0_sel:WORD_0 src1_sel:DWORD
	v_cmp_lt_i32_e32 vcc, v34, v37
	v_min_i32_e32 v2, v34, v37
	v_add_u32_e32 v2, v2, v35
	s_and_b64 vcc, vcc, s[24:25]
	s_or_b64 vcc, vcc, s[0:1]
	v_lshl_add_u64 v[32:33], v[2:3], 1, v[38:39]
	s_and_saveexec_b64 s[30:31], vcc
	global_store_short v[32:33], v28, off
	s_mov_b64 exec, s[30:31]
	v_addc_co_u32_e64 v35, vcc, 0, v35, s[0:1]
	v_addc_co_u32_e64 v34, vcc, 0, v34, s[24:25]
	s_mov_b64 s[0:1], 0x101
	v_lshl_add_u64 v[32:33], v[30:31], 0, s[0:1]
	v_cmp_gt_u32_sdwa s[0:1], v24, v36 src0_sel:WORD_1 src1_sel:DWORD
	v_cmp_eq_u32_sdwa s[24:25], v24, v36 src0_sel:WORD_1 src1_sel:DWORD
	v_cmp_lt_i32_e32 vcc, v34, v37
	v_min_i32_e32 v2, v34, v37
	v_add_u32_e32 v2, v2, v35
	s_and_b64 vcc, vcc, s[24:25]
	s_or_b64 vcc, vcc, s[0:1]
	v_lshl_add_u64 v[44:45], v[2:3], 1, v[38:39]
	s_and_saveexec_b64 s[30:31], vcc
	global_store_short v[44:45], v32, off
	s_mov_b64 exec, s[30:31]
	v_addc_co_u32_e64 v35, vcc, 0, v35, s[0:1]
	v_addc_co_u32_e64 v34, vcc, 0, v34, s[24:25]
	s_mov_b64 s[0:1], 0x102
	v_lshl_add_u64 v[32:33], v[30:31], 0, s[0:1]
	v_cmp_gt_u32_sdwa s[0:1], v25, v36 src0_sel:WORD_0 src1_sel:DWORD
	v_cmp_eq_u32_sdwa s[24:25], v25, v36 src0_sel:WORD_0 src1_sel:DWORD
	v_cmp_lt_i32_e32 vcc, v34, v37
	v_min_i32_e32 v2, v34, v37
	v_add_u32_e32 v2, v2, v35
	s_and_b64 vcc, vcc, s[24:25]
	s_or_b64 vcc, vcc, s[0:1]
	v_lshl_add_u64 v[44:45], v[2:3], 1, v[38:39]
	s_and_saveexec_b64 s[30:31], vcc
	global_store_short v[44:45], v32, off
	s_mov_b64 exec, s[30:31]
	v_addc_co_u32_e64 v35, vcc, 0, v35, s[0:1]
	v_addc_co_u32_e64 v34, vcc, 0, v34, s[24:25]
	s_mov_b64 s[0:1], 0x103
	v_lshl_add_u64 v[32:33], v[30:31], 0, s[0:1]
	v_cmp_gt_u32_sdwa s[0:1], v25, v36 src0_sel:WORD_1 src1_sel:DWORD
	v_cmp_eq_u32_sdwa s[24:25], v25, v36 src0_sel:WORD_1 src1_sel:DWORD
	v_cmp_lt_i32_e32 vcc, v34, v37
	v_min_i32_e32 v2, v34, v37
	v_add_u32_e32 v2, v2, v35
	s_and_b64 vcc, vcc, s[24:25]
	s_or_b64 vcc, vcc, s[0:1]
	v_lshl_add_u64 v[24:25], v[2:3], 1, v[38:39]
	s_and_saveexec_b64 s[30:31], vcc
	global_store_short v[24:25], v32, off
	s_mov_b64 exec, s[30:31]
	v_addc_co_u32_e64 v35, vcc, 0, v35, s[0:1]
	v_addc_co_u32_e64 v34, vcc, 0, v34, s[24:25]
	s_mov_b64 s[0:1], 0x104
	v_lshl_add_u64 v[24:25], v[30:31], 0, s[0:1]
	v_cmp_gt_u32_sdwa s[0:1], v26, v36 src0_sel:WORD_0 src1_sel:DWORD
	v_cmp_eq_u32_sdwa s[24:25], v26, v36 src0_sel:WORD_0 src1_sel:DWORD
	v_cmp_lt_i32_e32 vcc, v34, v37
	v_min_i32_e32 v2, v34, v37
	v_add_u32_e32 v2, v2, v35
	s_and_b64 vcc, vcc, s[24:25]
	s_or_b64 vcc, vcc, s[0:1]
	v_lshl_add_u64 v[32:33], v[2:3], 1, v[38:39]
	s_and_saveexec_b64 s[30:31], vcc
	global_store_short v[32:33], v24, off
	s_mov_b64 exec, s[30:31]
	v_addc_co_u32_e64 v35, vcc, 0, v35, s[0:1]
	v_addc_co_u32_e64 v34, vcc, 0, v34, s[24:25]
	s_mov_b64 s[0:1], 0x105
	v_lshl_add_u64 v[24:25], v[30:31], 0, s[0:1]
	v_cmp_gt_u32_sdwa s[0:1], v26, v36 src0_sel:WORD_1 src1_sel:DWORD
	v_cmp_eq_u32_sdwa s[24:25], v26, v36 src0_sel:WORD_1 src1_sel:DWORD
	v_cmp_lt_i32_e32 vcc, v34, v37
	v_min_i32_e32 v2, v34, v37
	v_add_u32_e32 v2, v2, v35
	s_and_b64 vcc, vcc, s[24:25]
	s_or_b64 vcc, vcc, s[0:1]
	v_lshl_add_u64 v[32:33], v[2:3], 1, v[38:39]
	s_and_saveexec_b64 s[30:31], vcc
	global_store_short v[32:33], v24, off
	s_mov_b64 exec, s[30:31]
	v_addc_co_u32_e64 v35, vcc, 0, v35, s[0:1]
	v_addc_co_u32_e64 v34, vcc, 0, v34, s[24:25]
	s_mov_b64 s[0:1], 0x106
	v_lshl_add_u64 v[24:25], v[30:31], 0, s[0:1]
	v_cmp_gt_u32_sdwa s[0:1], v27, v36 src0_sel:WORD_0 src1_sel:DWORD
	v_cmp_eq_u32_sdwa s[24:25], v27, v36 src0_sel:WORD_0 src1_sel:DWORD
	v_cmp_lt_i32_e32 vcc, v34, v37
	v_min_i32_e32 v2, v34, v37
	v_add_u32_e32 v2, v2, v35
	s_and_b64 vcc, vcc, s[24:25]
	s_or_b64 vcc, vcc, s[0:1]
	v_lshl_add_u64 v[32:33], v[2:3], 1, v[38:39]
	s_and_saveexec_b64 s[30:31], vcc
	global_store_short v[32:33], v24, off
	s_mov_b64 exec, s[30:31]
	v_addc_co_u32_e64 v35, vcc, 0, v35, s[0:1]
	v_addc_co_u32_e64 v34, vcc, 0, v34, s[24:25]
	s_mov_b64 s[0:1], 0x107
	v_lshl_add_u64 v[24:25], v[30:31], 0, s[0:1]
	v_cmp_gt_u32_sdwa s[0:1], v27, v36 src0_sel:WORD_1 src1_sel:DWORD
	v_cmp_eq_u32_sdwa s[24:25], v27, v36 src0_sel:WORD_1 src1_sel:DWORD
	v_cmp_lt_i32_e32 vcc, v34, v37
	v_min_i32_e32 v2, v34, v37
	v_add_u32_e32 v2, v2, v35
	s_and_b64 vcc, vcc, s[24:25]
	s_or_b64 vcc, vcc, s[0:1]
	v_lshl_add_u64 v[26:27], v[2:3], 1, v[38:39]
	s_and_saveexec_b64 s[30:31], vcc
	global_store_short v[26:27], v24, off
	s_mov_b64 exec, s[30:31]
	v_addc_co_u32_e64 v35, vcc, 0, v35, s[0:1]
	v_addc_co_u32_e64 v34, vcc, 0, v34, s[24:25]
	s_mov_b64 s[0:1], 0x108
	v_lshl_add_u64 v[24:25], v[30:31], 0, s[0:1]
	v_cmp_gt_u32_sdwa s[0:1], v20, v36 src0_sel:WORD_0 src1_sel:DWORD
	v_cmp_eq_u32_sdwa s[24:25], v20, v36 src0_sel:WORD_0 src1_sel:DWORD
	v_cmp_lt_i32_e32 vcc, v34, v37
	v_min_i32_e32 v2, v34, v37
	v_add_u32_e32 v2, v2, v35
	s_and_b64 vcc, vcc, s[24:25]
	s_or_b64 vcc, vcc, s[0:1]
	v_lshl_add_u64 v[26:27], v[2:3], 1, v[38:39]
	s_and_saveexec_b64 s[30:31], vcc
	global_store_short v[26:27], v24, off
	s_mov_b64 exec, s[30:31]
	v_addc_co_u32_e64 v35, vcc, 0, v35, s[0:1]
	v_addc_co_u32_e64 v34, vcc, 0, v34, s[24:25]
	s_mov_b64 s[0:1], 0x109
	v_lshl_add_u64 v[24:25], v[30:31], 0, s[0:1]
	v_cmp_gt_u32_sdwa s[0:1], v20, v36 src0_sel:WORD_1 src1_sel:DWORD
	v_cmp_eq_u32_sdwa s[24:25], v20, v36 src0_sel:WORD_1 src1_sel:DWORD
	v_cmp_lt_i32_e32 vcc, v34, v37
	v_min_i32_e32 v2, v34, v37
	v_add_u32_e32 v2, v2, v35
	s_and_b64 vcc, vcc, s[24:25]
	s_or_b64 vcc, vcc, s[0:1]
	v_lshl_add_u64 v[26:27], v[2:3], 1, v[38:39]
	s_and_saveexec_b64 s[30:31], vcc
	global_store_short v[26:27], v24, off
	s_mov_b64 exec, s[30:31]
	v_addc_co_u32_e64 v35, vcc, 0, v35, s[0:1]
	v_addc_co_u32_e64 v34, vcc, 0, v34, s[24:25]
	s_mov_b64 s[0:1], 0x10a
	v_lshl_add_u64 v[24:25], v[30:31], 0, s[0:1]
	v_cmp_gt_u32_sdwa s[0:1], v21, v36 src0_sel:WORD_0 src1_sel:DWORD
	v_cmp_eq_u32_sdwa s[24:25], v21, v36 src0_sel:WORD_0 src1_sel:DWORD
	v_cmp_lt_i32_e32 vcc, v34, v37
	v_min_i32_e32 v2, v34, v37
	v_add_u32_e32 v2, v2, v35
	s_and_b64 vcc, vcc, s[24:25]
	s_or_b64 vcc, vcc, s[0:1]
	v_lshl_add_u64 v[26:27], v[2:3], 1, v[38:39]
	s_and_saveexec_b64 s[30:31], vcc
	global_store_short v[26:27], v24, off
	s_mov_b64 exec, s[30:31]
	v_addc_co_u32_e64 v35, vcc, 0, v35, s[0:1]
	v_addc_co_u32_e64 v34, vcc, 0, v34, s[24:25]
	s_mov_b64 s[0:1], 0x10b
	v_lshl_add_u64 v[24:25], v[30:31], 0, s[0:1]
	v_cmp_gt_u32_sdwa s[0:1], v21, v36 src0_sel:WORD_1 src1_sel:DWORD
	v_cmp_eq_u32_sdwa s[24:25], v21, v36 src0_sel:WORD_1 src1_sel:DWORD
	v_cmp_lt_i32_e32 vcc, v34, v37
	v_min_i32_e32 v2, v34, v37
	v_add_u32_e32 v2, v2, v35
	s_and_b64 vcc, vcc, s[24:25]
	s_or_b64 vcc, vcc, s[0:1]
	v_lshl_add_u64 v[20:21], v[2:3], 1, v[38:39]
	s_and_saveexec_b64 s[30:31], vcc
	global_store_short v[20:21], v24, off
	s_mov_b64 exec, s[30:31]
	v_addc_co_u32_e64 v35, vcc, 0, v35, s[0:1]
	v_addc_co_u32_e64 v34, vcc, 0, v34, s[24:25]
	s_mov_b64 s[0:1], 0x10c
	v_lshl_add_u64 v[20:21], v[30:31], 0, s[0:1]
	v_cmp_gt_u32_sdwa s[0:1], v22, v36 src0_sel:WORD_0 src1_sel:DWORD
	v_cmp_eq_u32_sdwa s[24:25], v22, v36 src0_sel:WORD_0 src1_sel:DWORD
	v_cmp_lt_i32_e32 vcc, v34, v37
	v_min_i32_e32 v2, v34, v37
	v_add_u32_e32 v2, v2, v35
	s_and_b64 vcc, vcc, s[24:25]
	s_or_b64 vcc, vcc, s[0:1]
	v_lshl_add_u64 v[24:25], v[2:3], 1, v[38:39]
	s_and_saveexec_b64 s[30:31], vcc
	global_store_short v[24:25], v20, off
	s_mov_b64 exec, s[30:31]
	v_addc_co_u32_e64 v35, vcc, 0, v35, s[0:1]
	v_addc_co_u32_e64 v34, vcc, 0, v34, s[24:25]
	s_mov_b64 s[0:1], 0x10d
	v_lshl_add_u64 v[20:21], v[30:31], 0, s[0:1]
	v_cmp_gt_u32_sdwa s[0:1], v22, v36 src0_sel:WORD_1 src1_sel:DWORD
	v_cmp_eq_u32_sdwa s[24:25], v22, v36 src0_sel:WORD_1 src1_sel:DWORD
	v_cmp_lt_i32_e32 vcc, v34, v37
	v_min_i32_e32 v2, v34, v37
	v_add_u32_e32 v2, v2, v35
	s_and_b64 vcc, vcc, s[24:25]
	s_or_b64 vcc, vcc, s[0:1]
	v_lshl_add_u64 v[24:25], v[2:3], 1, v[38:39]
	s_and_saveexec_b64 s[30:31], vcc
	global_store_short v[24:25], v20, off
	s_mov_b64 exec, s[30:31]
	v_addc_co_u32_e64 v35, vcc, 0, v35, s[0:1]
	v_addc_co_u32_e64 v34, vcc, 0, v34, s[24:25]
	s_mov_b64 s[0:1], 0x10e
	v_lshl_add_u64 v[20:21], v[30:31], 0, s[0:1]
	v_cmp_gt_u32_sdwa s[0:1], v23, v36 src0_sel:WORD_0 src1_sel:DWORD
	v_cmp_eq_u32_sdwa s[24:25], v23, v36 src0_sel:WORD_0 src1_sel:DWORD
	v_cmp_lt_i32_e32 vcc, v34, v37
	v_min_i32_e32 v2, v34, v37
	v_add_u32_e32 v2, v2, v35
	s_and_b64 vcc, vcc, s[24:25]
	s_or_b64 vcc, vcc, s[0:1]
	v_lshl_add_u64 v[24:25], v[2:3], 1, v[38:39]
	s_and_saveexec_b64 s[30:31], vcc
	global_store_short v[24:25], v20, off
	s_mov_b64 exec, s[30:31]
	v_addc_co_u32_e64 v35, vcc, 0, v35, s[0:1]
	v_addc_co_u32_e64 v34, vcc, 0, v34, s[24:25]
	v_cmp_le_u32_sdwa s[24:25], v23, v36 src0_sel:WORD_1 src1_sel:DWORD
	s_mov_b64 s[0:1], 0
	s_and_saveexec_b64 s[30:31], s[24:25]
	s_xor_b64 s[24:25], exec, s[30:31]
	s_cbranch_execz .LBB0_1232
	v_cmp_eq_u32_sdwa s[0:1], v23, v36 src0_sel:WORD_1 src1_sel:DWORD
	v_cmp_lt_i32_e32 vcc, v34, v37
	s_and_b64 s[34:35], s[0:1], vcc
	s_mov_b64 s[0:1], 0
	s_and_saveexec_b64 s[30:31], s[34:35]
	v_add_u32_e32 v2, v34, v35
	s_mov_b64 s[0:1], exec
	v_mov_b64_e32 v[20:21], v[2:3]
	s_or_b64 exec, exec, s[30:31]
	s_and_b64 s[0:1], s[0:1], exec
	s_andn2_saveexec_b64 s[24:25], s[24:25]
	s_cbranch_execnz .LBB0_1233

.LBB0_976:
	ds_read_u16 v2, v50 offset:36928
	s_waitcnt lgkmcnt(0)
	v_cmp_ne_u16_e32 vcc, 0, v2
	s_and_saveexec_b64 s[18:19], vcc
	s_cbranch_execz .LBB0_1103
	ds_read_u16 v2, v49 offset:36928
	s_waitcnt vmcnt(5)
	v_add_u32_e32 v20, 0x11240, v49
	ds_read_b32 v20, v20
	v_lshl_add_u64 v[22:23], v[40:41], 0, s[16:17]
	s_mov_b64 s[0:1], 0x200
	s_waitcnt lgkmcnt(1)
	v_lshrrev_b32_e32 v21, 8, v2
	v_and_b32_e32 v2, 0xff, v2
	v_cndmask_b32_e64 v21, v21, 0, s[22:23]
	v_cndmask_b32_e64 v2, v2, 0, s[22:23]
	s_waitcnt vmcnt(4) lgkmcnt(0)
	v_add_u32_sdwa v26, v21, v20 dst_sel:DWORD dst_unused:UNUSED_PAD src0_sel:DWORD src1_sel:WORD_1
	v_add_u32_sdwa v27, v2, v20 dst_sel:DWORD dst_unused:UNUSED_PAD src0_sel:DWORD src1_sel:WORD_0
	v_lshl_add_u64 v[20:21], v[22:23], 0, s[0:1]
	s_waitcnt vmcnt(2)
	v_cmp_gt_u32_sdwa s[0:1], v16, v36 src0_sel:WORD_0 src1_sel:DWORD
	v_cmp_eq_u32_sdwa s[24:25], v16, v36 src0_sel:WORD_0 src1_sel:DWORD
	v_cmp_lt_i32_e32 vcc, v26, v37
	v_min_i32_e32 v2, v26, v37
	v_add_u32_e32 v2, v2, v27
	s_and_b64 vcc, vcc, s[24:25]
	s_or_b64 vcc, vcc, s[0:1]
	v_lshl_add_u64 v[24:25], v[2:3], 1, v[38:39]
	s_and_saveexec_b64 s[28:29], vcc
	global_store_short v[24:25], v20, off
	s_mov_b64 exec, s[28:29]
	v_addc_co_u32_e64 v27, vcc, 0, v27, s[0:1]
	v_addc_co_u32_e64 v26, vcc, 0, v26, s[24:25]
	s_mov_b64 s[0:1], 0x201
	v_lshl_add_u64 v[24:25], v[22:23], 0, s[0:1]
	v_cmp_gt_u32_sdwa s[0:1], v16, v36 src0_sel:WORD_1 src1_sel:DWORD
	v_cmp_eq_u32_sdwa s[24:25], v16, v36 src0_sel:WORD_1 src1_sel:DWORD
	v_cmp_lt_i32_e32 vcc, v26, v37
	v_min_i32_e32 v2, v26, v37
	v_add_u32_e32 v2, v2, v27
	s_and_b64 vcc, vcc, s[24:25]
	s_or_b64 vcc, vcc, s[0:1]
	v_lshl_add_u64 v[28:29], v[2:3], 1, v[38:39]
	s_and_saveexec_b64 s[28:29], vcc
	global_store_short v[28:29], v24, off
	s_mov_b64 exec, s[28:29]
	v_addc_co_u32_e64 v27, vcc, 0, v27, s[0:1]
	v_addc_co_u32_e64 v26, vcc, 0, v26, s[24:25]
	s_mov_b64 s[0:1], 0x202
	v_lshl_add_u64 v[24:25], v[22:23], 0, s[0:1]
	v_cmp_gt_u32_sdwa s[0:1], v17, v36 src0_sel:WORD_0 src1_sel:DWORD
	v_cmp_eq_u32_sdwa s[24:25], v17, v36 src0_sel:WORD_0 src1_sel:DWORD
	v_cmp_lt_i32_e32 vcc, v26, v37
	v_min_i32_e32 v2, v26, v37
	v_add_u32_e32 v2, v2, v27
	s_and_b64 vcc, vcc, s[24:25]
	s_or_b64 vcc, vcc, s[0:1]
	v_lshl_add_u64 v[28:29], v[2:3], 1, v[38:39]
	s_and_saveexec_b64 s[28:29], vcc
	global_store_short v[28:29], v24, off
	s_mov_b64 exec, s[28:29]
	v_addc_co_u32_e64 v27, vcc, 0, v27, s[0:1]
	v_addc_co_u32_e64 v26, vcc, 0, v26, s[24:25]
	s_mov_b64 s[0:1], 0x203
	v_lshl_add_u64 v[24:25], v[22:23], 0, s[0:1]
	v_cmp_gt_u32_sdwa s[0:1], v17, v36 src0_sel:WORD_1 src1_sel:DWORD
	v_cmp_eq_u32_sdwa s[24:25], v17, v36 src0_sel:WORD_1 src1_sel:DWORD
	v_cmp_lt_i32_e32 vcc, v26, v37
	v_min_i32_e32 v2, v26, v37
	v_add_u32_e32 v2, v2, v27
	s_and_b64 vcc, vcc, s[24:25]
	s_or_b64 vcc, vcc, s[0:1]
	v_lshl_add_u64 v[16:17], v[2:3], 1, v[38:39]
	s_and_saveexec_b64 s[28:29], vcc
	global_store_short v[16:17], v24, off
	s_mov_b64 exec, s[28:29]
	v_addc_co_u32_e64 v27, vcc, 0, v27, s[0:1]
	v_addc_co_u32_e64 v26, vcc, 0, v26, s[24:25]
	s_mov_b64 s[0:1], 0x204
	v_lshl_add_u64 v[16:17], v[22:23], 0, s[0:1]
	v_cmp_gt_u32_sdwa s[0:1], v18, v36 src0_sel:WORD_0 src1_sel:DWORD
	v_cmp_eq_u32_sdwa s[24:25], v18, v36 src0_sel:WORD_0 src1_sel:DWORD
	v_cmp_lt_i32_e32 vcc, v26, v37
	v_min_i32_e32 v2, v26, v37
	v_add_u32_e32 v2, v2, v27
	s_and_b64 vcc, vcc, s[24:25]
	s_or_b64 vcc, vcc, s[0:1]
	v_lshl_add_u64 v[24:25], v[2:3], 1, v[38:39]
	s_and_saveexec_b64 s[28:29], vcc
	global_store_short v[24:25], v16, off
	s_mov_b64 exec, s[28:29]
	v_addc_co_u32_e64 v27, vcc, 0, v27, s[0:1]
	v_addc_co_u32_e64 v26, vcc, 0, v26, s[24:25]
	s_mov_b64 s[0:1], 0x205
	v_lshl_add_u64 v[16:17], v[22:23], 0, s[0:1]
	v_cmp_gt_u32_sdwa s[0:1], v18, v36 src0_sel:WORD_1 src1_sel:DWORD
	v_cmp_eq_u32_sdwa s[24:25], v18, v36 src0_sel:WORD_1 src1_sel:DWORD
	v_cmp_lt_i32_e32 vcc, v26, v37
	v_min_i32_e32 v2, v26, v37
	v_add_u32_e32 v2, v2, v27
	s_and_b64 vcc, vcc, s[24:25]
	s_or_b64 vcc, vcc, s[0:1]
	v_lshl_add_u64 v[24:25], v[2:3], 1, v[38:39]
	s_and_saveexec_b64 s[28:29], vcc
	global_store_short v[24:25], v16, off
	s_mov_b64 exec, s[28:29]
	v_addc_co_u32_e64 v27, vcc, 0, v27, s[0:1]
	v_addc_co_u32_e64 v26, vcc, 0, v26, s[24:25]
	s_mov_b64 s[0:1], 0x206
	v_lshl_add_u64 v[16:17], v[22:23], 0, s[0:1]
	v_cmp_gt_u32_sdwa s[0:1], v19, v36 src0_sel:WORD_0 src1_sel:DWORD
	v_cmp_eq_u32_sdwa s[24:25], v19, v36 src0_sel:WORD_0 src1_sel:DWORD
	v_cmp_lt_i32_e32 vcc, v26, v37
	v_min_i32_e32 v2, v26, v37
	v_add_u32_e32 v2, v2, v27
	s_and_b64 vcc, vcc, s[24:25]
	s_or_b64 vcc, vcc, s[0:1]
	v_lshl_add_u64 v[24:25], v[2:3], 1, v[38:39]
	s_and_saveexec_b64 s[28:29], vcc
	global_store_short v[24:25], v16, off
	s_mov_b64 exec, s[28:29]
	v_addc_co_u32_e64 v27, vcc, 0, v27, s[0:1]
	v_addc_co_u32_e64 v26, vcc, 0, v26, s[24:25]
	s_mov_b64 s[0:1], 0x207
	v_lshl_add_u64 v[16:17], v[22:23], 0, s[0:1]
	v_cmp_gt_u32_sdwa s[0:1], v19, v36 src0_sel:WORD_1 src1_sel:DWORD
	v_cmp_eq_u32_sdwa s[24:25], v19, v36 src0_sel:WORD_1 src1_sel:DWORD
	v_cmp_lt_i32_e32 vcc, v26, v37
	v_min_i32_e32 v2, v26, v37
	v_add_u32_e32 v2, v2, v27
	s_and_b64 vcc, vcc, s[24:25]
	s_or_b64 vcc, vcc, s[0:1]
	v_lshl_add_u64 v[18:19], v[2:3], 1, v[38:39]
	s_and_saveexec_b64 s[28:29], vcc
	global_store_short v[18:19], v16, off
	s_mov_b64 exec, s[28:29]
	v_addc_co_u32_e64 v27, vcc, 0, v27, s[0:1]
	v_addc_co_u32_e64 v26, vcc, 0, v26, s[24:25]
	s_mov_b64 s[0:1], 0x208
	v_lshl_add_u64 v[16:17], v[22:23], 0, s[0:1]
	v_cmp_gt_u32_sdwa s[0:1], v12, v36 src0_sel:WORD_0 src1_sel:DWORD
	v_cmp_eq_u32_sdwa s[24:25], v12, v36 src0_sel:WORD_0 src1_sel:DWORD
	v_cmp_lt_i32_e32 vcc, v26, v37
	v_min_i32_e32 v2, v26, v37
	v_add_u32_e32 v2, v2, v27
	s_and_b64 vcc, vcc, s[24:25]
	s_or_b64 vcc, vcc, s[0:1]
	v_lshl_add_u64 v[18:19], v[2:3], 1, v[38:39]
	s_and_saveexec_b64 s[28:29], vcc
	global_store_short v[18:19], v16, off
	s_mov_b64 exec, s[28:29]
	v_addc_co_u32_e64 v27, vcc, 0, v27, s[0:1]
	v_addc_co_u32_e64 v26, vcc, 0, v26, s[24:25]
	s_mov_b64 s[0:1], 0x209
	v_lshl_add_u64 v[16:17], v[22:23], 0, s[0:1]
	v_cmp_gt_u32_sdwa s[0:1], v12, v36 src0_sel:WORD_1 src1_sel:DWORD
	v_cmp_eq_u32_sdwa s[24:25], v12, v36 src0_sel:WORD_1 src1_sel:DWORD
	v_cmp_lt_i32_e32 vcc, v26, v37
	v_min_i32_e32 v2, v26, v37
	v_add_u32_e32 v2, v2, v27
	s_and_b64 vcc, vcc, s[24:25]
	s_or_b64 vcc, vcc, s[0:1]
	v_lshl_add_u64 v[18:19], v[2:3], 1, v[38:39]
	s_and_saveexec_b64 s[28:29], vcc
	global_store_short v[18:19], v16, off
	s_mov_b64 exec, s[28:29]
	v_addc_co_u32_e64 v27, vcc, 0, v27, s[0:1]
	v_addc_co_u32_e64 v26, vcc, 0, v26, s[24:25]
	s_mov_b64 s[0:1], 0x20a
	v_lshl_add_u64 v[16:17], v[22:23], 0, s[0:1]
	v_cmp_gt_u32_sdwa s[0:1], v13, v36 src0_sel:WORD_0 src1_sel:DWORD
	v_cmp_eq_u32_sdwa s[24:25], v13, v36 src0_sel:WORD_0 src1_sel:DWORD
	v_cmp_lt_i32_e32 vcc, v26, v37
	v_min_i32_e32 v2, v26, v37
	v_add_u32_e32 v2, v2, v27
	s_and_b64 vcc, vcc, s[24:25]
	s_or_b64 vcc, vcc, s[0:1]
	v_lshl_add_u64 v[18:19], v[2:3], 1, v[38:39]
	s_and_saveexec_b64 s[28:29], vcc
	global_store_short v[18:19], v16, off
	s_mov_b64 exec, s[28:29]
	v_addc_co_u32_e64 v27, vcc, 0, v27, s[0:1]
	v_addc_co_u32_e64 v26, vcc, 0, v26, s[24:25]
	s_mov_b64 s[0:1], 0x20b
	v_lshl_add_u64 v[16:17], v[22:23], 0, s[0:1]
	v_cmp_gt_u32_sdwa s[0:1], v13, v36 src0_sel:WORD_1 src1_sel:DWORD
	v_cmp_eq_u32_sdwa s[24:25], v13, v36 src0_sel:WORD_1 src1_sel:DWORD
	v_cmp_lt_i32_e32 vcc, v26, v37
	v_min_i32_e32 v2, v26, v37
	v_add_u32_e32 v2, v2, v27
	s_and_b64 vcc, vcc, s[24:25]
	s_or_b64 vcc, vcc, s[0:1]
	v_lshl_add_u64 v[12:13], v[2:3], 1, v[38:39]
	s_and_saveexec_b64 s[28:29], vcc
	global_store_short v[12:13], v16, off
	s_mov_b64 exec, s[28:29]
	v_addc_co_u32_e64 v27, vcc, 0, v27, s[0:1]
	v_addc_co_u32_e64 v26, vcc, 0, v26, s[24:25]
	s_mov_b64 s[0:1], 0x20c
	v_lshl_add_u64 v[12:13], v[22:23], 0, s[0:1]
	v_cmp_gt_u32_sdwa s[0:1], v14, v36 src0_sel:WORD_0 src1_sel:DWORD
	v_cmp_eq_u32_sdwa s[24:25], v14, v36 src0_sel:WORD_0 src1_sel:DWORD
	v_cmp_lt_i32_e32 vcc, v26, v37
	v_min_i32_e32 v2, v26, v37
	v_add_u32_e32 v2, v2, v27
	s_and_b64 vcc, vcc, s[24:25]
	s_or_b64 vcc, vcc, s[0:1]
	v_lshl_add_u64 v[16:17], v[2:3], 1, v[38:39]
	s_and_saveexec_b64 s[28:29], vcc
	global_store_short v[16:17], v12, off
	s_mov_b64 exec, s[28:29]
	v_addc_co_u32_e64 v27, vcc, 0, v27, s[0:1]
	v_addc_co_u32_e64 v26, vcc, 0, v26, s[24:25]
	s_mov_b64 s[0:1], 0x20d
	v_lshl_add_u64 v[12:13], v[22:23], 0, s[0:1]
	v_cmp_gt_u32_sdwa s[0:1], v14, v36 src0_sel:WORD_1 src1_sel:DWORD
	v_cmp_eq_u32_sdwa s[24:25], v14, v36 src0_sel:WORD_1 src1_sel:DWORD
	v_cmp_lt_i32_e32 vcc, v26, v37
	v_min_i32_e32 v2, v26, v37
	v_add_u32_e32 v2, v2, v27
	s_and_b64 vcc, vcc, s[24:25]
	s_or_b64 vcc, vcc, s[0:1]
	v_lshl_add_u64 v[16:17], v[2:3], 1, v[38:39]
	s_and_saveexec_b64 s[28:29], vcc
	global_store_short v[16:17], v12, off
	s_mov_b64 exec, s[28:29]
	v_addc_co_u32_e64 v27, vcc, 0, v27, s[0:1]
	v_addc_co_u32_e64 v26, vcc, 0, v26, s[24:25]
	s_mov_b64 s[0:1], 0x20e
	v_lshl_add_u64 v[12:13], v[22:23], 0, s[0:1]
	v_cmp_gt_u32_sdwa s[0:1], v15, v36 src0_sel:WORD_0 src1_sel:DWORD
	v_cmp_eq_u32_sdwa s[24:25], v15, v36 src0_sel:WORD_0 src1_sel:DWORD
	v_cmp_lt_i32_e32 vcc, v26, v37
	v_min_i32_e32 v2, v26, v37
	v_add_u32_e32 v2, v2, v27
	s_and_b64 vcc, vcc, s[24:25]
	s_or_b64 vcc, vcc, s[0:1]
	v_lshl_add_u64 v[16:17], v[2:3], 1, v[38:39]
	s_and_saveexec_b64 s[28:29], vcc
	global_store_short v[16:17], v12, off
	s_mov_b64 exec, s[28:29]
	v_addc_co_u32_e64 v27, vcc, 0, v27, s[0:1]
	v_addc_co_u32_e64 v26, vcc, 0, v26, s[24:25]
	v_cmp_le_u32_sdwa s[24:25], v15, v36 src0_sel:WORD_1 src1_sel:DWORD
	s_mov_b64 s[0:1], 0
	s_and_saveexec_b64 s[28:29], s[24:25]
	s_xor_b64 s[24:25], exec, s[28:29]
	s_cbranch_execz .LBB0_1234
	v_cmp_eq_u32_sdwa s[0:1], v15, v36 src0_sel:WORD_1 src1_sel:DWORD
	v_cmp_lt_i32_e32 vcc, v26, v37
	s_and_b64 s[30:31], s[0:1], vcc
	s_mov_b64 s[0:1], 0
	s_and_saveexec_b64 s[28:29], s[30:31]
	v_add_u32_e32 v2, v26, v27
	s_mov_b64 s[0:1], exec
	v_mov_b64_e32 v[12:13], v[2:3]
	s_or_b64 exec, exec, s[28:29]
	s_and_b64 s[0:1], s[0:1], exec
	s_andn2_saveexec_b64 s[24:25], s[24:25]
	s_cbranch_execnz .LBB0_1235

.LBB0_1104:
	ds_read_u16 v2, v50 offset:36960
	s_waitcnt lgkmcnt(0)
	v_cmp_ne_u16_e32 vcc, 0, v2
	s_and_saveexec_b64 s[18:19], vcc
	s_cbranch_execz .LBB0_710
	ds_read_u16 v2, v49 offset:36960
	s_waitcnt vmcnt(3)
	v_add_u32_e32 v12, 0x11260, v49
	ds_read_b32 v12, v12
	v_lshl_add_u64 v[14:15], v[40:41], 0, s[16:17]
	s_mov_b64 s[0:1], 0x300
	s_waitcnt lgkmcnt(1)
	v_lshrrev_b32_e32 v13, 8, v2
	v_and_b32_e32 v2, 0xff, v2
	v_cndmask_b32_e64 v13, v13, 0, s[22:23]
	v_cndmask_b32_e64 v2, v2, 0, s[22:23]
	s_waitcnt vmcnt(2) lgkmcnt(0)
	v_add_u32_sdwa v18, v13, v12 dst_sel:DWORD dst_unused:UNUSED_PAD src0_sel:DWORD src1_sel:WORD_1
	v_add_u32_sdwa v19, v2, v12 dst_sel:DWORD dst_unused:UNUSED_PAD src0_sel:DWORD src1_sel:WORD_0
	v_lshl_add_u64 v[12:13], v[14:15], 0, s[0:1]
	s_waitcnt vmcnt(0)
	v_cmp_gt_u32_sdwa s[0:1], v8, v36 src0_sel:WORD_0 src1_sel:DWORD
	v_cmp_eq_u32_sdwa s[24:25], v8, v36 src0_sel:WORD_0 src1_sel:DWORD
	v_cmp_lt_i32_e32 vcc, v18, v37
	v_min_i32_e32 v2, v18, v37
	v_add_u32_e32 v2, v2, v19
	s_and_b64 vcc, vcc, s[24:25]
	s_or_b64 vcc, vcc, s[0:1]
	v_lshl_add_u64 v[16:17], v[2:3], 1, v[38:39]
	s_and_saveexec_b64 s[26:27], vcc
	global_store_short v[16:17], v12, off
	s_mov_b64 exec, s[26:27]
	v_addc_co_u32_e64 v19, vcc, 0, v19, s[0:1]
	v_addc_co_u32_e64 v18, vcc, 0, v18, s[24:25]
	s_mov_b64 s[0:1], 0x301
	v_lshl_add_u64 v[16:17], v[14:15], 0, s[0:1]
	v_cmp_gt_u32_sdwa s[0:1], v8, v36 src0_sel:WORD_1 src1_sel:DWORD
	v_cmp_eq_u32_sdwa s[24:25], v8, v36 src0_sel:WORD_1 src1_sel:DWORD
	v_cmp_lt_i32_e32 vcc, v18, v37
	v_min_i32_e32 v2, v18, v37
	v_add_u32_e32 v2, v2, v19
	s_and_b64 vcc, vcc, s[24:25]
	s_or_b64 vcc, vcc, s[0:1]
	v_lshl_add_u64 v[20:21], v[2:3], 1, v[38:39]
	s_and_saveexec_b64 s[26:27], vcc
	global_store_short v[20:21], v16, off
	s_mov_b64 exec, s[26:27]
	v_addc_co_u32_e64 v19, vcc, 0, v19, s[0:1]
	v_addc_co_u32_e64 v18, vcc, 0, v18, s[24:25]
	s_mov_b64 s[0:1], 0x302
	v_lshl_add_u64 v[16:17], v[14:15], 0, s[0:1]
	v_cmp_gt_u32_sdwa s[0:1], v9, v36 src0_sel:WORD_0 src1_sel:DWORD
	v_cmp_eq_u32_sdwa s[24:25], v9, v36 src0_sel:WORD_0 src1_sel:DWORD
	v_cmp_lt_i32_e32 vcc, v18, v37
	v_min_i32_e32 v2, v18, v37
	v_add_u32_e32 v2, v2, v19
	s_and_b64 vcc, vcc, s[24:25]
	s_or_b64 vcc, vcc, s[0:1]
	v_lshl_add_u64 v[20:21], v[2:3], 1, v[38:39]
	s_and_saveexec_b64 s[26:27], vcc
	global_store_short v[20:21], v16, off
	s_mov_b64 exec, s[26:27]
	v_addc_co_u32_e64 v19, vcc, 0, v19, s[0:1]
	v_addc_co_u32_e64 v18, vcc, 0, v18, s[24:25]
	s_mov_b64 s[0:1], 0x303
	v_lshl_add_u64 v[16:17], v[14:15], 0, s[0:1]
	v_cmp_gt_u32_sdwa s[0:1], v9, v36 src0_sel:WORD_1 src1_sel:DWORD
	v_cmp_eq_u32_sdwa s[24:25], v9, v36 src0_sel:WORD_1 src1_sel:DWORD
	v_cmp_lt_i32_e32 vcc, v18, v37
	v_min_i32_e32 v2, v18, v37
	v_add_u32_e32 v2, v2, v19
	s_and_b64 vcc, vcc, s[24:25]
	s_or_b64 vcc, vcc, s[0:1]
	v_lshl_add_u64 v[8:9], v[2:3], 1, v[38:39]
	s_and_saveexec_b64 s[26:27], vcc
	global_store_short v[8:9], v16, off
	s_mov_b64 exec, s[26:27]
	v_addc_co_u32_e64 v19, vcc, 0, v19, s[0:1]
	v_addc_co_u32_e64 v18, vcc, 0, v18, s[24:25]
	s_mov_b64 s[0:1], 0x304
	v_lshl_add_u64 v[8:9], v[14:15], 0, s[0:1]
	v_cmp_gt_u32_sdwa s[0:1], v10, v36 src0_sel:WORD_0 src1_sel:DWORD
	v_cmp_eq_u32_sdwa s[24:25], v10, v36 src0_sel:WORD_0 src1_sel:DWORD
	v_cmp_lt_i32_e32 vcc, v18, v37
	v_min_i32_e32 v2, v18, v37
	v_add_u32_e32 v2, v2, v19
	s_and_b64 vcc, vcc, s[24:25]
	s_or_b64 vcc, vcc, s[0:1]
	v_lshl_add_u64 v[16:17], v[2:3], 1, v[38:39]
	s_and_saveexec_b64 s[26:27], vcc
	global_store_short v[16:17], v8, off
	s_mov_b64 exec, s[26:27]
	v_addc_co_u32_e64 v19, vcc, 0, v19, s[0:1]
	v_addc_co_u32_e64 v18, vcc, 0, v18, s[24:25]
	s_mov_b64 s[0:1], 0x305
	v_lshl_add_u64 v[8:9], v[14:15], 0, s[0:1]
	v_cmp_gt_u32_sdwa s[0:1], v10, v36 src0_sel:WORD_1 src1_sel:DWORD
	v_cmp_eq_u32_sdwa s[24:25], v10, v36 src0_sel:WORD_1 src1_sel:DWORD
	v_cmp_lt_i32_e32 vcc, v18, v37
	v_min_i32_e32 v2, v18, v37
	v_add_u32_e32 v2, v2, v19
	s_and_b64 vcc, vcc, s[24:25]
	s_or_b64 vcc, vcc, s[0:1]
	v_lshl_add_u64 v[16:17], v[2:3], 1, v[38:39]
	s_and_saveexec_b64 s[26:27], vcc
	global_store_short v[16:17], v8, off
	s_mov_b64 exec, s[26:27]
	v_addc_co_u32_e64 v19, vcc, 0, v19, s[0:1]
	v_addc_co_u32_e64 v18, vcc, 0, v18, s[24:25]
	s_mov_b64 s[0:1], 0x306
	v_lshl_add_u64 v[8:9], v[14:15], 0, s[0:1]
	v_cmp_gt_u32_sdwa s[0:1], v11, v36 src0_sel:WORD_0 src1_sel:DWORD
	v_cmp_eq_u32_sdwa s[24:25], v11, v36 src0_sel:WORD_0 src1_sel:DWORD
	v_cmp_lt_i32_e32 vcc, v18, v37
	v_min_i32_e32 v2, v18, v37
	v_add_u32_e32 v2, v2, v19
	s_and_b64 vcc, vcc, s[24:25]
	s_or_b64 vcc, vcc, s[0:1]
	v_lshl_add_u64 v[16:17], v[2:3], 1, v[38:39]
	s_and_saveexec_b64 s[26:27], vcc
	global_store_short v[16:17], v8, off
	s_mov_b64 exec, s[26:27]
	v_addc_co_u32_e64 v19, vcc, 0, v19, s[0:1]
	v_addc_co_u32_e64 v18, vcc, 0, v18, s[24:25]
	s_mov_b64 s[0:1], 0x307
	v_lshl_add_u64 v[8:9], v[14:15], 0, s[0:1]
	v_cmp_gt_u32_sdwa s[0:1], v11, v36 src0_sel:WORD_1 src1_sel:DWORD
	v_cmp_eq_u32_sdwa s[24:25], v11, v36 src0_sel:WORD_1 src1_sel:DWORD
	v_cmp_lt_i32_e32 vcc, v18, v37
	v_min_i32_e32 v2, v18, v37
	v_add_u32_e32 v2, v2, v19
	s_and_b64 vcc, vcc, s[24:25]
	s_or_b64 vcc, vcc, s[0:1]
	v_lshl_add_u64 v[10:11], v[2:3], 1, v[38:39]
	s_and_saveexec_b64 s[26:27], vcc
	global_store_short v[10:11], v8, off
	s_mov_b64 exec, s[26:27]
	v_addc_co_u32_e64 v19, vcc, 0, v19, s[0:1]
	v_addc_co_u32_e64 v18, vcc, 0, v18, s[24:25]
	s_mov_b64 s[0:1], 0x308
	v_lshl_add_u64 v[8:9], v[14:15], 0, s[0:1]
	v_cmp_gt_u32_sdwa s[0:1], v4, v36 src0_sel:WORD_0 src1_sel:DWORD
	v_cmp_eq_u32_sdwa s[24:25], v4, v36 src0_sel:WORD_0 src1_sel:DWORD
	v_cmp_lt_i32_e32 vcc, v18, v37
	v_min_i32_e32 v2, v18, v37
	v_add_u32_e32 v2, v2, v19
	s_and_b64 vcc, vcc, s[24:25]
	s_or_b64 vcc, vcc, s[0:1]
	v_lshl_add_u64 v[10:11], v[2:3], 1, v[38:39]
	s_and_saveexec_b64 s[26:27], vcc
	global_store_short v[10:11], v8, off
	s_mov_b64 exec, s[26:27]
	v_addc_co_u32_e64 v19, vcc, 0, v19, s[0:1]
	v_addc_co_u32_e64 v18, vcc, 0, v18, s[24:25]
	s_mov_b64 s[0:1], 0x309
	v_lshl_add_u64 v[8:9], v[14:15], 0, s[0:1]
	v_cmp_gt_u32_sdwa s[0:1], v4, v36 src0_sel:WORD_1 src1_sel:DWORD
	v_cmp_eq_u32_sdwa s[24:25], v4, v36 src0_sel:WORD_1 src1_sel:DWORD
	v_cmp_lt_i32_e32 vcc, v18, v37
	v_min_i32_e32 v2, v18, v37
	v_add_u32_e32 v2, v2, v19
	s_and_b64 vcc, vcc, s[24:25]
	s_or_b64 vcc, vcc, s[0:1]
	v_lshl_add_u64 v[10:11], v[2:3], 1, v[38:39]
	s_and_saveexec_b64 s[26:27], vcc
	global_store_short v[10:11], v8, off
	s_mov_b64 exec, s[26:27]
	v_addc_co_u32_e64 v19, vcc, 0, v19, s[0:1]
	v_addc_co_u32_e64 v18, vcc, 0, v18, s[24:25]
	s_mov_b64 s[0:1], 0x30a
	v_lshl_add_u64 v[8:9], v[14:15], 0, s[0:1]
	v_cmp_gt_u32_sdwa s[0:1], v5, v36 src0_sel:WORD_0 src1_sel:DWORD
	v_cmp_eq_u32_sdwa s[24:25], v5, v36 src0_sel:WORD_0 src1_sel:DWORD
	v_cmp_lt_i32_e32 vcc, v18, v37
	v_min_i32_e32 v2, v18, v37
	v_add_u32_e32 v2, v2, v19
	s_and_b64 vcc, vcc, s[24:25]
	s_or_b64 vcc, vcc, s[0:1]
	v_lshl_add_u64 v[10:11], v[2:3], 1, v[38:39]
	s_and_saveexec_b64 s[26:27], vcc
	global_store_short v[10:11], v8, off
	s_mov_b64 exec, s[26:27]
	v_addc_co_u32_e64 v19, vcc, 0, v19, s[0:1]
	v_addc_co_u32_e64 v18, vcc, 0, v18, s[24:25]
	s_mov_b64 s[0:1], 0x30b
	v_lshl_add_u64 v[8:9], v[14:15], 0, s[0:1]
	v_cmp_gt_u32_sdwa s[0:1], v5, v36 src0_sel:WORD_1 src1_sel:DWORD
	v_cmp_eq_u32_sdwa s[24:25], v5, v36 src0_sel:WORD_1 src1_sel:DWORD
	v_cmp_lt_i32_e32 vcc, v18, v37
	v_min_i32_e32 v2, v18, v37
	v_add_u32_e32 v2, v2, v19
	s_and_b64 vcc, vcc, s[24:25]
	s_or_b64 vcc, vcc, s[0:1]
	v_lshl_add_u64 v[4:5], v[2:3], 1, v[38:39]
	s_and_saveexec_b64 s[26:27], vcc
	global_store_short v[4:5], v8, off
	s_mov_b64 exec, s[26:27]
	v_addc_co_u32_e64 v19, vcc, 0, v19, s[0:1]
	v_addc_co_u32_e64 v18, vcc, 0, v18, s[24:25]
	s_mov_b64 s[0:1], 0x30c
	v_lshl_add_u64 v[4:5], v[14:15], 0, s[0:1]
	v_cmp_gt_u32_sdwa s[0:1], v6, v36 src0_sel:WORD_0 src1_sel:DWORD
	v_cmp_eq_u32_sdwa s[24:25], v6, v36 src0_sel:WORD_0 src1_sel:DWORD
	v_cmp_lt_i32_e32 vcc, v18, v37
	v_min_i32_e32 v2, v18, v37
	v_add_u32_e32 v2, v2, v19
	s_and_b64 vcc, vcc, s[24:25]
	s_or_b64 vcc, vcc, s[0:1]
	v_lshl_add_u64 v[8:9], v[2:3], 1, v[38:39]
	s_and_saveexec_b64 s[26:27], vcc
	global_store_short v[8:9], v4, off
	s_mov_b64 exec, s[26:27]
	v_addc_co_u32_e64 v19, vcc, 0, v19, s[0:1]
	v_addc_co_u32_e64 v18, vcc, 0, v18, s[24:25]
	s_mov_b64 s[0:1], 0x30d
	v_lshl_add_u64 v[4:5], v[14:15], 0, s[0:1]
	v_cmp_gt_u32_sdwa s[0:1], v6, v36 src0_sel:WORD_1 src1_sel:DWORD
	v_cmp_eq_u32_sdwa s[24:25], v6, v36 src0_sel:WORD_1 src1_sel:DWORD
	v_cmp_lt_i32_e32 vcc, v18, v37
	v_min_i32_e32 v2, v18, v37
	v_add_u32_e32 v2, v2, v19
	s_and_b64 vcc, vcc, s[24:25]
	s_or_b64 vcc, vcc, s[0:1]
	v_lshl_add_u64 v[8:9], v[2:3], 1, v[38:39]
	s_and_saveexec_b64 s[26:27], vcc
	global_store_short v[8:9], v4, off
	s_mov_b64 exec, s[26:27]
	v_addc_co_u32_e64 v19, vcc, 0, v19, s[0:1]
	v_addc_co_u32_e64 v18, vcc, 0, v18, s[24:25]
	s_mov_b64 s[0:1], 0x30e
	v_lshl_add_u64 v[4:5], v[14:15], 0, s[0:1]
	v_cmp_gt_u32_sdwa s[0:1], v7, v36 src0_sel:WORD_0 src1_sel:DWORD
	v_cmp_eq_u32_sdwa s[24:25], v7, v36 src0_sel:WORD_0 src1_sel:DWORD
	v_cmp_lt_i32_e32 vcc, v18, v37
	v_min_i32_e32 v2, v18, v37
	v_add_u32_e32 v2, v2, v19
	s_and_b64 vcc, vcc, s[24:25]
	s_or_b64 vcc, vcc, s[0:1]
	v_lshl_add_u64 v[8:9], v[2:3], 1, v[38:39]
	s_and_saveexec_b64 s[26:27], vcc
	global_store_short v[8:9], v4, off
	s_mov_b64 exec, s[26:27]
	v_addc_co_u32_e64 v19, vcc, 0, v19, s[0:1]
	v_addc_co_u32_e64 v18, vcc, 0, v18, s[24:25]
	v_cmp_le_u32_sdwa s[24:25], v7, v36 src0_sel:WORD_1 src1_sel:DWORD
	s_mov_b64 s[0:1], 0
	s_and_saveexec_b64 s[26:27], s[24:25]
	s_xor_b64 s[24:25], exec, s[26:27]
	s_cbranch_execz .LBB0_1236
	v_cmp_eq_u32_sdwa s[0:1], v7, v36 src0_sel:WORD_1 src1_sel:DWORD
	v_cmp_lt_i32_e32 vcc, v18, v37
	s_and_b64 s[28:29], s[0:1], vcc
	s_mov_b64 s[0:1], 0
	s_and_saveexec_b64 s[26:27], s[28:29]
	v_add_u32_e32 v2, v18, v19
	s_mov_b64 s[0:1], exec
	v_mov_b64_e32 v[4:5], v[2:3]
	s_or_b64 exec, exec, s[26:27]
	s_and_b64 s[0:1], s[0:1], exec
	s_andn2_saveexec_b64 s[24:25], s[24:25]
	s_cbranch_execnz .LBB0_1237
